# s8
# speedup vs baseline: 1.0078x; 1.0078x over previous
.LBB0_14:
	s_or_b64 exec, exec, s[0:1]
	v_lshlrev_b64 v[82:83], 8, v[88:89]
	v_lshl_add_u64 v[82:83], s[12:13], 0, v[82:83]
	s_mov_b64 s[0:1], 0x164000
	v_lshl_add_u64 v[88:89], v[82:83], 0, s[0:1]
	v_lshlrev_b32_e32 v90, 2, v105
	s_and_saveexec_b64 s[0:1], s[8:9]
	s_cbranch_execz .LBB0_16
	v_mul_u32_u24_e32 v94, 43, v105
	v_lshrrev_b32_e32 v94, 9, v94
	v_mul_u32_u24_e32 v94, 12, v94
	v_sub_u32_e32 v95, v105, v94
	v_and_b32_e32 v91, 3, v95
	v_lshrrev_b32_e32 v95, 2, v95
	v_mad_u32_u24 v91, v91, 3, v95
	v_add_u32_e32 v91, v91, v94
	v_lshlrev_b32_e32 v94, 2, v91
	v_mov_b32_e32 v95, 0
	v_lshl_add_u64 v[94:95], v[88:89], 0, v[94:95]
	s_waitcnt vmcnt(26)
	global_store_dword v[94:95], v114, off

_Z11attn_kernelILi4EEvPKfS1_S1_S1_S1_S1_PKcPf:
	s_load_dwordx2 s[24:25], s[0:1], 0x30
	s_load_dwordx8 s[8:15], s[0:1], 0x0
	s_load_dwordx4 s[16:19], s[0:1], 0x20
	v_lshrrev_b32_e32 v63, 6, v0
	v_and_b32_e32 v57, 15, v0
	v_bfe_u32 v1, v0, 4, 2
	v_lshrrev_b32_e32 v2, 2, v57
	v_mul_u32_u24_e32 v4, 3, v1
	v_mul_u32_u24_e32 v2, 3, v2
	v_mad_u32_u24 v4, v63, 12, v4
	v_mad_u32_u24 v2, v63, 12, v2
	v_lshlrev_b32_e32 v4, 2, v4
	v_lshlrev_b32_e32 v2, 2, v2
	v_and_b32_e32 v104, 63, v0
	v_lshlrev_b32_e32 v60, 5, v57
	v_lshlrev_b32_e32 v58, 3, v1
	v_add_u32_e32 v3, v60, v58
	v_lshrrev_b32_e32 v56, 4, v0
	v_lshlrev_b32_e32 v54, 4, v57
	v_mov_b32_e32 v59, 0
	s_movk_i32 s4, 0xe0
	v_cmp_gt_u32_e64 s[4:5], s4, v0
	s_lshl_b32 s26, s2, 8
	s_lshl_b32 s27, s2, 9
	s_mul_i32 s28, s2, 14
	v_lshlrev_b32_e32 v5, 2, v57
	v_lshlrev_b32_e32 v147, 6, v57
	s_waitcnt lgkmcnt(0)
	s_add_u32 s20, s24, s26
	s_addc_u32 s21, s25, 0
	s_add_u32 s20, s20, 0x164000
	s_addc_u32 s21, s21, 0
	s_add_u32 s26, s24, s27
	s_addc_u32 s27, s25, 0
	s_add_u32 s26, s26, 0x80000
	s_addc_u32 s27, s27, 0
	global_load_dwordx3 v[80:82], v2, s[20:21]
	global_load_dwordx3 v[84:86], v4, s[20:21]
	global_load_dwordx2 v[64:65], v3, s[26:27]
	s_load_dword s3, s[20:21], 0xc0
	s_add_u32 s22, s24, 0x160000
	s_addc_u32 s23, s25, 0
	v_cndmask_b32_e64 v62, 13, v56, s[4:5]
	v_add_u32_e32 v3, s28, v62
	v_mad_u32_u24 v144, v3, 36, v5
	v_mad_u32_u24 v146, v3, 12, v5
	v_add_u32_e32 v145, -36, v146
	v_add_u32_e32 v146, -48, v146
	v_lshl_or_b32 v147, v63, 10, v147
	v_lshl_or_b32 v147, v1, 4, v147
	v_or_b32_e32 v148, 0x1000, v147
	v_lshlrev_b32_e32 v149, 4, v104
	v_lshlrev_b32_e32 v150, 9, v3
	v_add_u32_e32 v150, v150, v54
	v_and_b32_e32 v87, 3, v57
	v_lshlrev_b32_e32 v87, 4, v87
	v_lshl_or_b32 v87, v1, 6, v87
	v_lshlrev_b32_e32 v88, 3, v57
	s_add_u32 s26, s24, 0x100000
	s_addc_u32 s27, s25, 0
	s_add_u32 s28, s24, 0x140000
	s_addc_u32 s29, s25, 0
	s_waitcnt lgkmcnt(0)
	s_bitcmp0_b32 s3, 1
	s_cselect_b64 s[20:21], -1, 0
	s_cbranch_scc1 .LBB1_16
	s_waitcnt vmcnt(1)
	v_lshl_add_u32 v72, v80, 9, v87
	v_lshl_add_u32 v73, v81, 9, v87
	v_lshl_add_u32 v74, v82, 9, v87
	global_load_dwordx4 v[50:53], v72, s[24:25]
	global_load_dwordx4 v[46:49], v72, s[24:25] offset:256
	global_load_dwordx4 v[14:17], v73, s[24:25]
	global_load_dwordx4 v[10:13], v73, s[24:25] offset:256
	global_load_dwordx4 v[6:9], v74, s[24:25]
	global_load_dwordx4 v[2:5], v74, s[24:25] offset:256
	v_lshl_add_u32 v75, v84, 8, v54
	v_lshl_add_u32 v78, v84, 7, v88
	v_lshl_add_u32 v76, v85, 8, v54
	v_lshl_add_u32 v79, v85, 7, v88
	v_lshl_add_u32 v77, v86, 8, v54
	v_lshl_add_u32 v80, v86, 7, v88
	global_load_dwordx4 v[30:33], v75, s[26:27]
	global_load_dwordx2 v[70:71], v78, s[28:29]
	global_load_dwordx4 v[26:29], v76, s[26:27]
	global_load_dwordx2 v[66:67], v79, s[28:29]
	global_load_dwordx4 v[18:21], v77, s[26:27]
	global_load_dwordx2 v[68:69], v80, s[28:29]
	s_mov_b32 exec_lo, 0x1ff01ff
	s_mov_b32 exec_hi, 0x1ff01ff
	global_load_dword v120, v144, s[10:11]
	s_mov_b32 exec_lo, 0xe000e00
	s_mov_b32 exec_hi, 0xe000e00
	global_load_dword v120, v145, s[12:13]
	s_mov_b32 exec_lo, 0x70007000
	s_mov_b32 exec_hi, 0x70007000
	global_load_dword v120, v146, s[14:15]
	s_mov_b64 exec, -1
	global_load_dwordx4 v[124:127], v147, s[22:23]
	global_load_dwordx4 v[128:131], v148, s[22:23]
	s_mov_b32 exec_hi, 0
	global_load_dwordx4 v[132:135], v149, s[16:17]
	s_mov_b32 exec_hi, -1
	s_mov_b32 exec_lo, 0
	global_load_dwordx4 v[132:135], v149, s[18:19] offset:-512
	s_mov_b32 exec_lo, -1
	global_load_dwordx4 v[136:139], v150, s[8:9]
	global_load_dwordx4 v[140:143], v150, s[8:9] offset:256
	s_movk_i32 s6, 0x140
	v_cmp_gt_u32_e32 vcc, s6, v0
	v_lshlrev_b32_e32 v22, 2, v0
	v_mov_b32_e32 v23, 0
	s_and_saveexec_b64 s[6:7], vcc
	ds_write_b32 v22, v23 offset:14336
	s_or_b64 exec, exec, s[6:7]
	v_cmp_gt_u32_e32 vcc, 64, v0
	s_and_saveexec_b64 s[6:7], vcc
	ds_write_b32 v22, v23 offset:15360
	s_or_b64 exec, exec, s[6:7]
	v_bfe_u32 v22, s3, v57, 1
	v_cmp_eq_u32_e32 vcc, 0, v22
	v_mov_b32_e32 v45, 0xc9c35000
	s_mov_b32 s30, 0x3db8aa3b
	s_mov_b32 s31, 0x3db8aa3b
	v_cndmask_b32_e64 v55, 1.0, 0, vcc
	v_mov_b32_e32 v121, 0x3fb8aa3b
	s_bitcmp0_b32 s3, 0
	s_cselect_b64 vcc, -1, 0
	v_cndmask_b32_e32 v34, 0, v45, vcc
	s_bitcmp0_b32 s3, 2
	s_cselect_b64 vcc, -1, 0
	v_cndmask_b32_e32 v36, 0, v45, vcc
	s_bitcmp0_b32 s3, 3
	s_cselect_b64 vcc, -1, 0
	v_cndmask_b32_e32 v37, 0, v45, vcc
	s_bitcmp0_b32 s3, 4
	s_cselect_b64 vcc, -1, 0
	v_cndmask_b32_e32 v22, 0, v45, vcc
	s_bitcmp0_b32 s3, 5
	s_cselect_b64 vcc, -1, 0
	v_cndmask_b32_e32 v23, 0, v45, vcc
	s_bitcmp0_b32 s3, 6
	s_cselect_b64 vcc, -1, 0
	v_cndmask_b32_e32 v24, 0, v45, vcc
	s_bitcmp0_b32 s3, 7
	s_cselect_b64 vcc, -1, 0
	v_cndmask_b32_e32 v25, 0, v45, vcc
	s_bitcmp0_b32 s3, 8
	s_cselect_b64 vcc, -1, 0
	v_cndmask_b32_e32 v38, 0, v45, vcc
	s_bitcmp0_b32 s3, 9
	s_cselect_b64 vcc, -1, 0
	v_cndmask_b32_e32 v39, 0, v45, vcc
	s_bitcmp0_b32 s3, 10
	s_cselect_b64 vcc, -1, 0
	v_cndmask_b32_e32 v40, 0, v45, vcc
	s_bitcmp0_b32 s3, 11
	s_cselect_b64 vcc, -1, 0
	v_cndmask_b32_e32 v41, 0, v45, vcc
	s_bitcmp0_b32 s3, 12
	s_cselect_b64 vcc, -1, 0
	v_cndmask_b32_e32 v42, 0, v45, vcc
	s_bitcmp0_b32 s3, 13
	s_cselect_b64 vcc, -1, 0
	v_cndmask_b32_e32 v43, 0, v45, vcc
	v_mov_b32_e32 v35, 0
	v_mov_b32_e32 v44, v45
	v_mov_b32_e32 v75, 0
	v_mov_b32_e32 v79, 0
	v_mov_b32_e32 v83, 0
	s_waitcnt vmcnt(20)
	v_mfma_f32_16x16x32_fp8_fp8 v[160:163], v[50:51], v[64:65], v[34:37]
	v_mfma_f32_16x16x32_fp8_fp8 v[164:167], v[52:53], v[64:65], v[22:25]
	s_waitcnt vmcnt(19)
	v_mfma_f32_16x16x32_fp8_fp8 v[168:171], v[46:47], v[64:65], v[38:41]
	v_mfma_f32_16x16x32_fp8_fp8 v[172:175], v[48:49], v[64:65], v[42:45]
	s_nop 3
	v_max3_f32 v86, v160, v161, v162
	v_max3_f32 v87, v163, v164, v165
	v_max3_f32 v88, v166, v167, v168
	v_max3_f32 v89, v169, v170, v171
	v_max3_f32 v86, v86, v172, v173
	v_max3_f32 v87, v87, v88, v89
	v_max_f32_e32 v96, v86, v87
	v_mul_f32_e32 v98, 0xbdb8aa3b, v96
	v_pk_fma_f32 v[208:209], v[160:161], s[30:31], v[98:99] op_sel_hi:[1,1,0]
	v_pk_fma_f32 v[210:211], v[162:163], s[30:31], v[98:99] op_sel_hi:[1,1,0]
	v_pk_fma_f32 v[212:213], v[164:165], s[30:31], v[98:99] op_sel_hi:[1,1,0]
	v_pk_fma_f32 v[214:215], v[166:167], s[30:31], v[98:99] op_sel_hi:[1,1,0]
	v_pk_fma_f32 v[216:217], v[168:169], s[30:31], v[98:99] op_sel_hi:[1,1,0]
	v_pk_fma_f32 v[218:219], v[170:171], s[30:31], v[98:99] op_sel_hi:[1,1,0]
	v_pk_fma_f32 v[220:221], v[172:173], s[30:31], v[98:99] op_sel_hi:[1,1,0]
	v_exp_f32_e32 v208, v208
	v_exp_f32_e32 v209, v209
	v_exp_f32_e32 v210, v210
	v_exp_f32_e32 v211, v211
	v_exp_f32_e32 v212, v212
	v_exp_f32_e32 v213, v213
	v_exp_f32_e32 v214, v214
	v_exp_f32_e32 v215, v215
	v_exp_f32_e32 v216, v216
	v_exp_f32_e32 v217, v217
	v_exp_f32_e32 v218, v218
	v_exp_f32_e32 v219, v219
	v_exp_f32_e32 v220, v220
	v_exp_f32_e32 v221, v221
	s_waitcnt vmcnt(18)
	v_mfma_f32_16x16x32_fp8_fp8 v[176:179], v[14:15], v[64:65], v[34:37]
	v_mfma_f32_16x16x32_fp8_fp8 v[180:183], v[16:17], v[64:65], v[22:25]
	s_waitcnt vmcnt(17)
	v_mfma_f32_16x16x32_fp8_fp8 v[184:187], v[10:11], v[64:65], v[38:41]
	v_mfma_f32_16x16x32_fp8_fp8 v[188:191], v[12:13], v[64:65], v[42:45]
	v_pk_add_f32 v[86:87], v[208:209], v[210:211]
	v_pk_add_f32 v[88:89], v[212:213], v[214:215]
	v_pk_add_f32 v[90:91], v[216:217], v[218:219]
	v_pk_mul_f32 v[92:93], v[208:209], v[160:161]
	v_pk_mul_f32 v[94:95], v[210:211], v[162:163]
	v_pk_add_f32 v[86:87], v[86:87], v[220:221]
	v_pk_add_f32 v[88:89], v[88:89], v[90:91]
	v_pk_fma_f32 v[92:93], v[212:213], v[164:165], v[92:93]
	v_pk_fma_f32 v[94:95], v[214:215], v[166:167], v[94:95]
	v_pk_add_f32 v[86:87], v[86:87], v[88:89]
	v_pk_fma_f32 v[92:93], v[216:217], v[168:169], v[92:93]
	v_pk_fma_f32 v[94:95], v[218:219], v[170:171], v[94:95]
	v_add_f32_e32 v86, v86, v87
	v_pk_fma_f32 v[92:93], v[220:221], v[172:173], v[92:93]
	v_rcp_f32_e32 v87, v86
	v_pk_add_f32 v[92:93], v[92:93], v[94:95]
	v_mul_f32_e32 v87, v55, v87
	v_add_f32_e32 v92, v92, v93
	v_mul_f32_e32 v107, v86, v87
	v_mul_f32_e32 v92, v92, v87
	v_mul_f32_e32 v100, 0x43800000, v87
	v_mul_f32_e32 v103, 0x3d800000, v92
	v_max3_f32 v86, v176, v177, v178
	v_max3_f32 v87, v179, v180, v181
	v_max3_f32 v88, v182, v183, v184
	v_max3_f32 v89, v185, v186, v187
	v_max3_f32 v86, v86, v188, v189
	v_max3_f32 v87, v87, v88, v89
	v_max_f32_e32 v96, v86, v87
	v_mul_f32_e32 v98, 0xbdb8aa3b, v96
	v_pk_fma_f32 v[222:223], v[176:177], s[30:31], v[98:99] op_sel_hi:[1,1,0]
	v_pk_fma_f32 v[224:225], v[178:179], s[30:31], v[98:99] op_sel_hi:[1,1,0]
	v_pk_fma_f32 v[226:227], v[180:181], s[30:31], v[98:99] op_sel_hi:[1,1,0]
	v_pk_fma_f32 v[228:229], v[182:183], s[30:31], v[98:99] op_sel_hi:[1,1,0]
	v_pk_fma_f32 v[230:231], v[184:185], s[30:31], v[98:99] op_sel_hi:[1,1,0]
	v_pk_fma_f32 v[232:233], v[186:187], s[30:31], v[98:99] op_sel_hi:[1,1,0]
	v_pk_fma_f32 v[234:235], v[188:189], s[30:31], v[98:99] op_sel_hi:[1,1,0]
	v_exp_f32_e32 v222, v222
	v_exp_f32_e32 v223, v223
	v_exp_f32_e32 v224, v224
	v_exp_f32_e32 v225, v225
	v_exp_f32_e32 v226, v226
	v_exp_f32_e32 v227, v227
	v_exp_f32_e32 v228, v228
	v_exp_f32_e32 v229, v229
	v_exp_f32_e32 v230, v230
	v_exp_f32_e32 v231, v231
	v_exp_f32_e32 v232, v232
	v_exp_f32_e32 v233, v233
	v_exp_f32_e32 v234, v234
	v_exp_f32_e32 v235, v235
	s_waitcnt vmcnt(16)
	v_mfma_f32_16x16x32_fp8_fp8 v[192:195], v[6:7], v[64:65], v[34:37]
	v_mfma_f32_16x16x32_fp8_fp8 v[196:199], v[8:9], v[64:65], v[22:25]
	s_waitcnt vmcnt(15)
	v_mfma_f32_16x16x32_fp8_fp8 v[200:203], v[2:3], v[64:65], v[38:41]
	v_mfma_f32_16x16x32_fp8_fp8 v[204:207], v[4:5], v[64:65], v[42:45]
	v_pk_add_f32 v[86:87], v[222:223], v[224:225]
	v_pk_add_f32 v[88:89], v[226:227], v[228:229]
	v_pk_add_f32 v[90:91], v[230:231], v[232:233]
	v_pk_mul_f32 v[92:93], v[222:223], v[176:177]
	v_pk_mul_f32 v[94:95], v[224:225], v[178:179]
	v_pk_add_f32 v[86:87], v[86:87], v[234:235]
	v_pk_add_f32 v[88:89], v[88:89], v[90:91]
	v_pk_fma_f32 v[92:93], v[226:227], v[180:181], v[92:93]
	v_pk_fma_f32 v[94:95], v[228:229], v[182:183], v[94:95]
	v_pk_add_f32 v[86:87], v[86:87], v[88:89]
	v_pk_fma_f32 v[92:93], v[230:231], v[184:185], v[92:93]
	v_pk_fma_f32 v[94:95], v[232:233], v[186:187], v[94:95]
	v_add_f32_e32 v86, v86, v87
	v_pk_fma_f32 v[92:93], v[234:235], v[188:189], v[92:93]
	v_rcp_f32_e32 v87, v86
	v_pk_add_f32 v[92:93], v[92:93], v[94:95]
	v_mul_f32_e32 v87, v55, v87
	v_add_f32_e32 v92, v92, v93
	v_mul_f32_e32 v108, v86, v87
	v_mul_f32_e32 v92, v92, v87
	v_mul_f32_e32 v101, 0x43800000, v87
	v_mul_f32_e32 v105, 0x3d800000, v92
	v_max3_f32 v86, v192, v193, v194
	v_max3_f32 v87, v195, v196, v197
	v_max3_f32 v88, v198, v199, v200
	v_max3_f32 v89, v201, v202, v203
	v_max3_f32 v86, v86, v204, v205
	v_max3_f32 v87, v87, v88, v89
	v_max_f32_e32 v96, v86, v87
	v_mul_f32_e32 v98, 0xbdb8aa3b, v96
	v_pk_fma_f32 v[236:237], v[192:193], s[30:31], v[98:99] op_sel_hi:[1,1,0]
	v_pk_fma_f32 v[238:239], v[194:195], s[30:31], v[98:99] op_sel_hi:[1,1,0]
	v_pk_fma_f32 v[240:241], v[196:197], s[30:31], v[98:99] op_sel_hi:[1,1,0]
	v_pk_fma_f32 v[242:243], v[198:199], s[30:31], v[98:99] op_sel_hi:[1,1,0]
	v_pk_fma_f32 v[244:245], v[200:201], s[30:31], v[98:99] op_sel_hi:[1,1,0]
	v_pk_fma_f32 v[246:247], v[202:203], s[30:31], v[98:99] op_sel_hi:[1,1,0]
	v_pk_fma_f32 v[248:249], v[204:205], s[30:31], v[98:99] op_sel_hi:[1,1,0]
	v_exp_f32_e32 v236, v236
	v_exp_f32_e32 v237, v237
	v_exp_f32_e32 v238, v238
	v_exp_f32_e32 v239, v239
	v_exp_f32_e32 v240, v240
	v_exp_f32_e32 v241, v241
	v_exp_f32_e32 v242, v242
	v_exp_f32_e32 v243, v243
	v_exp_f32_e32 v244, v244
	v_exp_f32_e32 v245, v245
	v_exp_f32_e32 v246, v246
	v_exp_f32_e32 v247, v247
	v_exp_f32_e32 v248, v248
	v_exp_f32_e32 v249, v249
	v_pk_add_f32 v[86:87], v[236:237], v[238:239]
	v_pk_add_f32 v[88:89], v[240:241], v[242:243]
	v_pk_add_f32 v[90:91], v[244:245], v[246:247]
	v_pk_mul_f32 v[92:93], v[236:237], v[192:193]
	v_pk_mul_f32 v[94:95], v[238:239], v[194:195]
	v_pk_add_f32 v[86:87], v[86:87], v[248:249]
	v_pk_add_f32 v[88:89], v[88:89], v[90:91]
	v_pk_fma_f32 v[92:93], v[240:241], v[196:197], v[92:93]
	v_pk_fma_f32 v[94:95], v[242:243], v[198:199], v[94:95]
	v_pk_add_f32 v[86:87], v[86:87], v[88:89]
	v_pk_fma_f32 v[92:93], v[244:245], v[200:201], v[92:93]
	v_pk_fma_f32 v[94:95], v[246:247], v[202:203], v[94:95]
	v_add_f32_e32 v86, v86, v87
	v_pk_fma_f32 v[92:93], v[248:249], v[204:205], v[92:93]
	v_rcp_f32_e32 v87, v86
	v_pk_add_f32 v[92:93], v[92:93], v[94:95]
	v_mul_f32_e32 v87, v55, v87
	v_add_f32_e32 v92, v92, v93
	v_mul_f32_e32 v109, v86, v87
	v_mul_f32_e32 v92, v92, v87
	v_mul_f32_e32 v102, 0x43800000, v87
	v_mul_f32_e32 v106, 0x3d800000, v92
	v_max3_f32 v122, v103, v105, v106
	v_cmp_gt_u32_e64 s[6:7], 16, v104
	v_mov_b32_e32 v123, v122
	s_nop 1
	v_permlane16_swap_b32_e32 v122, v123
	v_max_f32_e32 v122, v122, v123
	v_mov_b32_e32 v123, v122
	s_nop 1
	v_permlane32_swap_b32_e32 v122, v123
	v_max_f32_e32 v36, v122, v123
	v_mul_f32_e32 v123, 0x3fb8aa3b, v36
	v_fma_f32 v111, v103, v121, -v123
	v_exp_f32_e32 v111, v111
	s_nop 0
	v_mul_f32_e32 v112, v111, v100
	v_mul_f32_e32 v110, v111, v107
	v_mov_b32_e32 v114, v111
	v_pk_mul_f32 v[208:209], v[208:209], v[112:113] op_sel_hi:[1,0]
	v_pk_mul_f32 v[210:211], v[210:211], v[112:113] op_sel_hi:[1,0]
	v_pk_mul_f32 v[212:213], v[212:213], v[112:113] op_sel_hi:[1,0]
	v_pk_mul_f32 v[214:215], v[214:215], v[112:113] op_sel_hi:[1,0]
	v_pk_mul_f32 v[216:217], v[216:217], v[112:113] op_sel_hi:[1,0]
	v_pk_mul_f32 v[218:219], v[218:219], v[112:113] op_sel_hi:[1,0]
	v_pk_mul_f32 v[220:221], v[220:221], v[112:113] op_sel_hi:[1,0]
	s_waitcnt vmcnt(13)
	v_mov_b32_e32 v115, v110
	v_fma_mix_f32 v116, v110, v70, 0 op_sel_hi:[0,1,0]
	v_fma_mix_f32 v117, v110, v70, 0 op_sel:[0,1,0] op_sel_hi:[0,1,0]
	v_fma_mix_f32 v118, v110, v71, 0 op_sel_hi:[0,1,0]
	v_cvt_pk_fp8_f32 v72, v208, v209
	v_cvt_pk_fp8_f32 v73, v212, v213
	v_cvt_pk_fp8_f32 v74, v216, v217
	v_cvt_pk_fp8_f32 v75, v220, v221
	v_cvt_pk_fp8_f32 v72, v210, v211 op_sel:[0,0,1]
	v_cvt_pk_fp8_f32 v73, v214, v215 op_sel:[0,0,1]
	v_cvt_pk_fp8_f32 v74, v218, v219 op_sel:[0,0,1]
	s_nop 1
	v_mfma_f32_16x16x32_fp8_fp8 v[152:155], v[72:73], v[30:31], 0
	v_mfma_f32_16x16x32_fp8_fp8 v[152:155], v[74:75], v[32:33], v[152:155]
	v_fma_f32 v111, v105, v121, -v123
	v_exp_f32_e32 v111, v111
	s_nop 0
	v_mul_f32_e32 v112, v111, v101
	v_mul_f32_e32 v110, v111, v108
	v_add_f32_e32 v114, v114, v111
	v_pk_mul_f32 v[222:223], v[222:223], v[112:113] op_sel_hi:[1,0]
	v_pk_mul_f32 v[224:225], v[224:225], v[112:113] op_sel_hi:[1,0]
	v_pk_mul_f32 v[226:227], v[226:227], v[112:113] op_sel_hi:[1,0]
	v_pk_mul_f32 v[228:229], v[228:229], v[112:113] op_sel_hi:[1,0]
	v_pk_mul_f32 v[230:231], v[230:231], v[112:113] op_sel_hi:[1,0]
	v_pk_mul_f32 v[232:233], v[232:233], v[112:113] op_sel_hi:[1,0]
	v_pk_mul_f32 v[234:235], v[234:235], v[112:113] op_sel_hi:[1,0]
	s_waitcnt vmcnt(11)
	v_add_f32_e32 v115, v115, v110
	v_fma_mix_f32 v116, v110, v66, v116 op_sel_hi:[0,1,0]
	v_fma_mix_f32 v117, v110, v66, v117 op_sel:[0,1,0] op_sel_hi:[0,1,0]
	v_fma_mix_f32 v118, v110, v67, v118 op_sel_hi:[0,1,0]
	v_cvt_pk_fp8_f32 v76, v222, v223
	v_cvt_pk_fp8_f32 v77, v226, v227
	v_cvt_pk_fp8_f32 v78, v230, v231
	v_cvt_pk_fp8_f32 v79, v234, v235
	v_cvt_pk_fp8_f32 v76, v224, v225 op_sel:[0,0,1]
	v_cvt_pk_fp8_f32 v77, v228, v229 op_sel:[0,0,1]
	v_cvt_pk_fp8_f32 v78, v232, v233 op_sel:[0,0,1]
	s_nop 1
	v_mfma_f32_16x16x32_fp8_fp8 v[152:155], v[76:77], v[26:27], v[152:155]
	v_mfma_f32_16x16x32_fp8_fp8 v[152:155], v[78:79], v[28:29], v[152:155]
	v_fma_f32 v111, v106, v121, -v123
	v_exp_f32_e32 v111, v111
	s_nop 0
	v_mul_f32_e32 v112, v111, v102
	v_mul_f32_e32 v110, v111, v109
	v_add_f32_e32 v114, v114, v111
	v_pk_mul_f32 v[236:237], v[236:237], v[112:113] op_sel_hi:[1,0]
	v_pk_mul_f32 v[238:239], v[238:239], v[112:113] op_sel_hi:[1,0]
	v_pk_mul_f32 v[240:241], v[240:241], v[112:113] op_sel_hi:[1,0]
	v_pk_mul_f32 v[242:243], v[242:243], v[112:113] op_sel_hi:[1,0]
	v_pk_mul_f32 v[244:245], v[244:245], v[112:113] op_sel_hi:[1,0]
	v_pk_mul_f32 v[246:247], v[246:247], v[112:113] op_sel_hi:[1,0]
	v_pk_mul_f32 v[248:249], v[248:249], v[112:113] op_sel_hi:[1,0]
	s_waitcnt vmcnt(9)
	v_add_f32_e32 v115, v115, v110
	v_fma_mix_f32 v116, v110, v68, v116 op_sel_hi:[0,1,0]
	v_fma_mix_f32 v117, v110, v68, v117 op_sel:[0,1,0] op_sel_hi:[0,1,0]
	v_fma_mix_f32 v118, v110, v69, v118 op_sel_hi:[0,1,0]
	v_cvt_pk_fp8_f32 v80, v236, v237
	v_cvt_pk_fp8_f32 v81, v240, v241
	v_cvt_pk_fp8_f32 v82, v244, v245
	v_cvt_pk_fp8_f32 v83, v248, v249
	v_cvt_pk_fp8_f32 v80, v238, v239 op_sel:[0,0,1]
	v_cvt_pk_fp8_f32 v81, v242, v243 op_sel:[0,0,1]
	v_cvt_pk_fp8_f32 v82, v246, v247 op_sel:[0,0,1]
	s_nop 1
	v_mfma_f32_16x16x32_fp8_fp8 v[152:155], v[80:81], v[18:19], v[152:155]
	v_mfma_f32_16x16x32_fp8_fp8 v[152:155], v[82:83], v[20:21], v[152:155]
	v_mov_b32_e32 v86, v114
	v_mov_b32_e32 v87, v115
	v_mov_b32_e32 v88, v116
	v_mov_b32_e32 v89, v117
	v_mov_b32_e32 v90, v118
	v_permlane16_swap_b32_e32 v114, v86
	v_permlane16_swap_b32_e32 v115, v87
	v_permlane16_swap_b32_e32 v116, v88
	v_permlane16_swap_b32_e32 v117, v89
	v_permlane16_swap_b32_e32 v118, v90
	v_add_f32_e32 v114, v114, v86
	v_add_f32_e32 v115, v115, v87
	v_add_f32_e32 v116, v116, v88
	v_add_f32_e32 v117, v117, v89
	v_add_f32_e32 v118, v118, v90
	v_mov_b32_e32 v86, v114
	v_mov_b32_e32 v87, v115
	v_mov_b32_e32 v88, v116
	v_mov_b32_e32 v89, v117
	v_mov_b32_e32 v90, v118
	v_permlane32_swap_b32_e32 v114, v86
	v_permlane32_swap_b32_e32 v115, v87
	v_permlane32_swap_b32_e32 v116, v88
	v_permlane32_swap_b32_e32 v117, v89
	v_permlane32_swap_b32_e32 v118, v90
	v_mul_u32_u24_e32 v91, 0x140, v1
	s_movk_i32 s26, 0x500
	v_mad_u32_u24 v91, v63, s26, v91
	v_lshl_or_b32 v91, v57, 2, v91
	v_add_u32_e32 v91, 0x1c00, v91
	v_add_f32_e32 v37, v114, v86
	v_add_f32_e32 v20, v115, v87
	v_add_f32_e32 v18, v116, v88
	v_add_f32_e32 v19, v117, v89
	v_add_f32_e32 v21, v118, v90
	ds_write2_b32 v91, v152, v153 offset0:0 offset1:20
	ds_write2_b32 v91, v154, v155 offset0:40 offset1:60
	s_branch .LBB1_30

.LBB1_32:
	s_or_b64 exec, exec, s[8:9]
	s_movk_i32 s6, 0x100
	v_cmp_gt_u32_e64 s[6:7], s6, v0
	s_waitcnt lgkmcnt(0)
	s_barrier
	s_and_saveexec_b64 s[14:15], s[6:7]
	s_cbranch_execz .LBB1_39
	v_lshlrev_b32_e32 v21, 5, v56
	v_cmp_gt_u32_e32 vcc, 3, v57
	v_add_u32_e32 v37, 4, v57
	v_lshlrev_b32_e32 v19, 2, v57
	s_movk_i32 s8, 0x50
	v_cndmask_b32_e32 v37, 4, v37, vcc
	v_mad_u32_u24 v19, v56, s8, v19
	v_lshl_add_u32 v37, v37, 2, v21
	ds_read_b96 v[160:162], v21 offset:12288
	ds_read_b96 v[164:166], v21 offset:12800
	ds_read_b96 v[168:170], v21 offset:13312
	ds_read_b96 v[172:174], v21 offset:13824
	ds_read2st64_b32 v[176:177], v37 offset0:48 offset1:50
	ds_read2st64_b32 v[178:179], v37 offset0:52 offset1:54
	ds_read2st64_b32 v[180:181], v19 offset0:28 offset1:33
	ds_read2st64_b32 v[182:183], v19 offset0:38 offset1:43
	v_cndmask_b32_e64 v18, 1.0, 0, s[20:21]
	v_mul_u32_u24_e32 v20, 0x50, v56
	s_waitcnt lgkmcnt(4)
	v_max_f32_e32 v21, v160, v164
	v_max3_f32 v33, v21, v168, v172
	v_sub_f32_e32 v21, v160, v33
	v_sub_f32_e32 v29, v164, v33
	v_sub_f32_e32 v30, v168, v33
	v_sub_f32_e32 v33, v172, v33
	v_mul_f32_e32 v21, 0x3fb8aa3b, v21
	v_mul_f32_e32 v29, 0x3fb8aa3b, v29
	v_mul_f32_e32 v30, 0x3fb8aa3b, v30
	v_mul_f32_e32 v33, 0x3fb8aa3b, v33
	v_exp_f32_e32 v21, v21
	v_exp_f32_e32 v29, v29
	v_exp_f32_e32 v30, v30
	v_exp_f32_e32 v33, v33
	v_or_b32_e32 v20, 0x3800, v20
	v_mul_f32_e32 v35, v21, v161
	v_mul_f32_e32 v34, v21, v162
	v_fmac_f32_e32 v35, v29, v165
	v_fmac_f32_e32 v34, v29, v166
	v_fmac_f32_e32 v35, v30, v169
	v_fmac_f32_e32 v34, v30, v170
	v_fmac_f32_e32 v35, v33, v173
	v_fmac_f32_e32 v34, v33, v174
	v_rcp_f32_e32 v35, v35
	s_waitcnt lgkmcnt(0)
	v_mul_f32_e32 v31, v21, v180
	v_mul_f32_e32 v18, v18, v35
	v_fmac_f32_e32 v31, v29, v181
	v_mul_f32_e32 v35, v21, v176
	v_fmac_f32_e32 v31, v30, v182
	v_fmac_f32_e32 v35, v29, v177
	v_fmac_f32_e32 v31, v33, v183
	v_fmac_f32_e32 v35, v30, v178
	v_mul_f32_e32 v31, v31, v18
	v_fmac_f32_e32 v35, v33, v179
	s_mov_b32 s8, 0x3a800000
	v_lshl_add_u32 v36, v57, 1, v20
	v_fma_mixlo_f16 v31, v31, s8, 0
	v_cmp_eq_u32_e64 s[8:9], 7, v57
	s_and_saveexec_b64 s[10:11], s[4:5]
	ds_write_b16 v36, v31
	s_and_b64 exec, exec, s[8:9]
	v_mov_b32_e32 v31, 0x3c00
	ds_write_b16 v20, v31 offset:46
	s_or_b64 exec, exec, s[10:11]
	s_waitcnt vmcnt(6)
	v_mov_b32_dpp v33, v120 row_newbcast:10 row_mask:0xf bank_mask:0xf bound_ctrl:1
	v_mov_b32_dpp v36, v120 row_newbcast:11 row_mask:0xf bank_mask:0xf bound_ctrl:1
	v_cmp_eq_u32_e64 s[10:11], 1, v57
	v_mov_b32_dpp v32, v120 row_newbcast:9 row_mask:0xf bank_mask:0xf bound_ctrl:1
	v_mov_b32_dpp v38, v120 row_newbcast:13 row_mask:0xf bank_mask:0xf bound_ctrl:1
	v_mov_b32_dpp v39, v120 row_newbcast:14 row_mask:0xf bank_mask:0xf bound_ctrl:1
	v_cndmask_b32_e64 v33, v36, v33, s[10:11]
	v_cmp_eq_u32_e64 s[8:9], 0, v57
	v_mov_b32_dpp v37, v120 row_newbcast:12 row_mask:0xf bank_mask:0xf bound_ctrl:1
	v_mov_b32_dpp v27, v120 row_newbcast:0 row_mask:0xf bank_mask:0xf bound_ctrl:1
	v_cndmask_b32_e64 v32, v33, v32, s[8:9]
	v_cndmask_b32_e64 v33, v39, v38, s[10:11]
	v_cndmask_b32_e64 v33, v33, v37, s[8:9]
	v_fma_f32 v33, v34, v33, -v35
	v_fma_f32 v32, v18, v33, -v32
	v_mov_b32_dpp v20, v120 row_newbcast:1 row_mask:0xf bank_mask:0xf bound_ctrl:1
	v_mov_b32_dpp v19, v120 row_newbcast:2 row_mask:0xf bank_mask:0xf bound_ctrl:1
	v_mov_b32_dpp v31, v120 row_newbcast:3 row_mask:0xf bank_mask:0xf bound_ctrl:1
	v_mov_b32_dpp v29, v120 row_newbcast:4 row_mask:0xf bank_mask:0xf bound_ctrl:1
	v_mov_b32_dpp v26, v120 row_newbcast:5 row_mask:0xf bank_mask:0xf bound_ctrl:1
	v_mov_b32_dpp v30, v120 row_newbcast:6 row_mask:0xf bank_mask:0xf bound_ctrl:1
	v_mov_b32_dpp v28, v120 row_newbcast:7 row_mask:0xf bank_mask:0xf bound_ctrl:1
	v_mov_b32_dpp v21, v120 row_newbcast:8 row_mask:0xf bank_mask:0xf bound_ctrl:1
	v_mov_b32_dpp v18, v32 quad_perm:[0,0,0,0] row_mask:0xf bank_mask:0xf bound_ctrl:1
	v_mov_b32_dpp v33, v32 quad_perm:[1,1,1,1] row_mask:0xf bank_mask:0xf bound_ctrl:1
	v_mov_b32_dpp v32, v32 quad_perm:[2,2,2,2] row_mask:0xf bank_mask:0xf bound_ctrl:1
	s_and_b64 s[12:13], vcc, s[4:5]
	s_and_b64 exec, exec, s[12:13]
	s_cbranch_execz .LBB1_39
	v_mul_f32_e32 v31, v31, v33
	v_fmac_f32_e32 v31, v27, v18
	v_mul_f32_e32 v27, v29, v33
	v_fmac_f32_e32 v27, v20, v18
	v_fmac_f32_e32 v27, v28, v32
	v_mul_f32_e32 v20, v26, v33
	v_fmac_f32_e32 v31, v30, v32
	v_fmac_f32_e32 v20, v19, v18
	v_mul_f32_e32 v18, v27, v27
	v_fmac_f32_e32 v20, v21, v32
	v_fmac_f32_e32 v18, v31, v31
	v_fmac_f32_e32 v18, v20, v20
	v_mad_u32_u24 v26, v56, 3, v57
	v_sqrt_f32_e32 v18, v18
	v_cndmask_b32_e64 v19, v20, v27, s[10:11]
	v_add_u32_e32 v29, 56, v26
	v_add_f32_e32 v21, 0x38d1b717, v18
	v_rcp_f32_e32 v21, v21
	v_cndmask_b32_e64 v20, v19, v31, s[8:9]
	v_mul_u32_u24_e32 v28, 0x2493, v26
	v_mul_u32_u24_e32 v30, 0x2493, v29
	v_lshrrev_b32_e32 v28, 16, v28
	v_lshrrev_b32_e32 v30, 16, v30
	v_mul_u32_u24_e32 v28, 66, v28
	v_mul_u32_u24_e32 v30, 66, v30
	v_lshl_add_u32 v28, v26, 1, v28
	v_lshl_add_u32 v30, v29, 1, v30
	v_cvt_f16_f32_e32 v27, v20
	v_fma_mixlo_f16 v20, v20, v21, 0
	ds_write_b16 v28, v27 offset:14368
	ds_write_b16 v30, v20 offset:14368
	s_and_b64 exec, exec, s[8:9]
	s_cbranch_execz .LBB1_39
	v_cmp_lt_u32_e32 vcc, 6, v56
	v_cvt_f16_f32_e32 v18, v18
	v_lshlrev_b32_e32 v19, 1, v56
	v_mov_b32_e32 v20, 0x42
	v_cndmask_b32_e32 v20, 0, v20, vcc
	v_add_u32_e32 v19, v19, v20
	ds_write_b16 v19, v18 offset:14848
